# q/k/v finaliser: raw k and v row loads hoisted to the rope-table load point (4 dependent memory round trips per row instead of 5 become 2)
# speedup vs baseline: 1.0060x; 1.0006x over previous
.LBB0_1001:
	s_or_b64 exec, exec, s[18:19]
	v_mov_b32_e32 v192, 0
	v_mov_b32_e32 v193, 0
	v_mov_b32_e32 v194, 0
	v_mov_b32_e32 v195, 0
	v_mov_b32_e32 v196, 0
	v_mov_b32_e32 v197, 0
	v_mov_b32_e32 v198, 0
	v_mov_b32_e32 v199, 0
	v_mov_b32_e32 v200, 0
	v_mov_b32_e32 v201, 0
	v_mov_b32_e32 v202, 0
	v_mov_b32_e32 v203, 0
	v_lshl_add_u64 v[212:213], s[86:87], 0, v[70:71]
	v_lshl_add_u64 v[214:215], s[86:87], 0, v[72:73]
	s_and_saveexec_b64 s[42:43], s[6:7]
	s_and_saveexec_b64 s[44:45], s[10:11]
	s_xor_b64 s[44:45], exec, s[44:45]
	global_load_dwordx4 v[192:195], v[212:213], off offset:-1280
	global_load_dwordx4 v[196:199], v[212:213], off
	global_load_dwordx4 v[200:203], v[212:213], off offset:1280
	s_andn2_saveexec_b64 s[44:45], s[44:45]
	global_load_dwordx4 v[192:195], v[214:215], off
	global_load_dwordx4 v[196:199], v[214:215], off
	global_load_dwordx4 v[200:203], v[214:215], off
	s_or_b64 exec, exec, s[44:45]
	s_or_b64 exec, exec, s[42:43]
	v_lshl_add_u64 v[216:217], s[86:87], 0, v[78:79]
	global_load_dwordx4 v[204:207], v[216:217], off
	v_lshl_add_u64 v[216:217], s[86:87], 0, v[80:81]
	s_and_saveexec_b64 s[42:43], s[16:17]
	global_load_dwordx4 v[208:211], v[216:217], off
	s_or_b64 exec, exec, s[42:43]
	v_lshl_add_u64 v[90:91], s[86:87], 0, v[82:83]
	v_mov_b32_e32 v43, 0
	v_mov_b32_e32 v44, 0
	v_mov_b32_e32 v45, 0
	s_and_saveexec_b64 s[18:19], s[6:7]
	s_cbranch_execz .LBB0_1003
	global_load_dwordx4 v[42:45], v[90:91], off offset:-768

.LBB0_1015:
	s_or_b64 exec, exec, s[18:19]
	s_waitcnt lgkmcnt(1)
	v_mov_b32_e32 v42, v192
	v_mov_b32_e32 v43, v193
	v_mov_b32_e32 v44, v194
	v_mov_b32_e32 v45, v195
	v_mov_b32_e32 v38, v196
	v_mov_b32_e32 v39, v197
	v_mov_b32_e32 v40, v198
	v_mov_b32_e32 v41, v199
	v_mov_b32_e32 v34, v200
	v_mov_b32_e32 v35, v201
	v_mov_b32_e32 v36, v202
	v_mov_b32_e32 v37, v203
	v_mov_b32_e32 v87, 0
	v_mov_b32_e32 v94, 0
	v_mov_b32_e32 v92, 0
	v_mov_b32_e32 v93, 0
	v_mov_b32_e32 v90, 0
	s_waitcnt lgkmcnt(0)
	v_mov_b32_e32 v91, 0
	v_mov_b32_e32 v88, 0
	v_mov_b32_e32 v89, 0
	s_and_saveexec_b64 s[18:19], s[6:7]
	s_cbranch_execz .LBB0_1035
	v_lshlrev_b32_e32 v87, 16, v42
	v_and_b32_e32 v94, 0xffff0000, v42
	v_lshlrev_b32_e32 v92, 16, v43
	v_and_b32_e32 v93, 0xffff0000, v43
	v_lshlrev_b32_e32 v90, 16, v44
	v_and_b32_e32 v91, 0xffff0000, v44
	v_lshlrev_b32_e32 v88, 16, v45
	v_and_b32_e32 v89, 0xffff0000, v45
.LBB0_1035:
	s_or_b64 exec, exec, s[18:19]
	v_mul_f32_e32 v42, 0x4b800000, v86
	v_cndmask_b32_e32 v42, v86, v42, vcc
	v_rsq_f32_e32 v42, v42
	s_nop 0
	v_mul_f32_e32 v43, 0x45800000, v42
	v_cndmask_b32_e32 v46, v42, v43, vcc
	v_cndmask_b32_e64 v44, v46, 1.0, s[8:9]
	v_mul_f32_e32 v45, v44, v87
	v_mul_f32_e32 v94, v44, v94
	v_pk_mul_f32 v[42:43], v[44:45], v[92:93] op_sel_hi:[0,1]
	v_mul_f32_e32 v92, v94, v94
	v_pk_mul_f32 v[86:87], v[42:43], v[42:43]
	v_fmac_f32_e32 v92, v45, v45
	v_add_f32_e32 v86, v86, v92
	v_add_f32_e32 v92, v87, v86
	v_pk_mul_f32 v[86:87], v[44:45], v[90:91] op_sel_hi:[0,1]
	v_pk_mul_f32 v[90:91], v[86:87], v[86:87]
	v_pk_mul_f32 v[88:89], v[44:45], v[88:89] op_sel_hi:[0,1]
	v_add_f32_e32 v90, v90, v92
	v_add_f32_e32 v92, v91, v90
	v_pk_mul_f32 v[90:91], v[88:89], v[88:89]
	s_nop 0
	v_add_f32_e32 v90, v90, v92
	v_add_f32_e32 v90, v91, v90
	ds_bpermute_b32 v91, v110, v90
	s_waitcnt lgkmcnt(0)
	v_add_f32_e32 v90, v90, v91
	ds_bpermute_b32 v91, v111, v90
	s_waitcnt lgkmcnt(0)
	v_add_f32_e32 v90, v90, v91
	ds_bpermute_b32 v91, v112, v90
	s_waitcnt lgkmcnt(0)
	v_add_f32_e32 v90, v90, v91
	ds_bpermute_b32 v91, v113, v90
	s_waitcnt lgkmcnt(0)
	v_add_f32_e32 v90, v90, v91
	ds_bpermute_b32 v91, v114, v90
	s_waitcnt lgkmcnt(0)
	v_add_f32_e32 v90, v90, v91
	v_fmamk_f32 v90, v90, 0x3baaaaab, v68
	v_mul_f32_e32 v91, 0x4b800000, v90
	v_cmp_gt_f32_e32 vcc, s34, v90
	s_nop 1
	v_cndmask_b32_e32 v90, v90, v91, vcc
	v_rsq_f32_e32 v90, v90
	s_nop 0
	v_mul_f32_e32 v91, 0x45800000, v90
	v_cndmask_b32_e32 v90, v90, v91, vcc
	v_mul_f32_e32 v90, 0x3ea535b8, v90
	v_mul_f32_e32 v95, v16, v90
	v_mul_f32_e32 v91, v14, v90
	v_mul_f32_e32 v92, v15, v90
	v_mul_f32_e32 v117, v17, v90
	v_mul_f32_e32 v119, v6, v90
	v_mul_f32_e32 v121, v7, v90
	v_mul_f32_e32 v122, v8, v90
	v_mul_f32_e32 v95, v42, v95
	v_mul_f32_e32 v42, v9, v90
	v_mul_f32_e32 v45, v45, v91
	v_mul_f32_e32 v93, v94, v92
	v_mul_f32_e32 v118, v43, v117
	v_mul_f32_e32 v120, v86, v119
	v_mul_f32_e32 v124, v87, v121
	v_mul_f32_e32 v126, v88, v122
	v_mul_f32_e32 v129, v89, v42
	ds_bpermute_b32 v94, v111, v45
	ds_bpermute_b32 v117, v111, v93
	ds_bpermute_b32 v119, v111, v95
	ds_bpermute_b32 v123, v111, v118
	ds_bpermute_b32 v125, v111, v120
	ds_bpermute_b32 v127, v111, v124
	ds_bpermute_b32 v128, v111, v126
	ds_bpermute_b32 v130, v111, v129
	v_mov_b32_e32 v92, 0
	v_lshl_add_u64 v[42:43], s[86:87], 0, v[74:75]
	v_mov_b32_e32 v121, 0
	v_mov_b32_e32 v122, 0
	v_mov_b32_e32 v90, 0
	v_mov_b32_e32 v91, 0
	v_mov_b32_e32 v88, 0
	v_mov_b32_e32 v89, 0
	v_mov_b32_e32 v86, 0
	v_mov_b32_e32 v87, 0
	s_and_saveexec_b64 s[18:19], s[6:7]
	s_cbranch_execz .LBB0_1037
	s_waitcnt lgkmcnt(0)
	v_mul_f32_e32 v86, v33, v130
	v_mul_f32_e32 v91, v23, v119
	v_cndmask_b32_e64 v88, v86, -v86, s[12:13]
	v_mul_f32_e32 v86, v31, v128
	v_cndmask_b32_e64 v91, v91, -v91, s[12:13]
	v_cndmask_b32_e64 v89, v86, -v86, s[12:13]
	v_mul_f32_e32 v86, v29, v127
	v_fmac_f32_e32 v91, v22, v95
	v_mul_f32_e32 v95, v21, v117
	v_cndmask_b32_e64 v87, v86, -v86, s[12:13]
	v_mul_f32_e32 v86, v27, v125
	v_cndmask_b32_e64 v95, v95, -v95, s[12:13]
	v_cndmask_b32_e64 v90, v86, -v86, s[12:13]
	v_mul_f32_e32 v86, v25, v123
	v_fmac_f32_e32 v95, v20, v93
	v_mul_f32_e32 v93, v19, v94
	v_cndmask_b32_e64 v86, v86, -v86, s[12:13]
	v_cndmask_b32_e64 v93, v93, -v93, s[12:13]
	v_fmac_f32_e32 v86, v24, v118
	v_fmac_f32_e32 v93, v18, v45
	v_fmac_f32_e32 v87, v28, v124
	v_fmac_f32_e32 v90, v26, v120
	v_med3_f32 v45, v93, s35, v109
	v_med3_f32 v93, v95, s35, v109
	v_med3_f32 v94, v86, s35, v109
	v_mov_b32_e32 v86, v47
	v_cvt_pk_fp8_f32 v86, v45, v93
	v_med3_f32 v45, v90, s35, v109
	v_med3_f32 v90, v87, s35, v109
	v_mov_b32_e32 v87, v47
	v_cvt_pk_fp8_f32 v87, v45, v90
	v_fmac_f32_e32 v88, v32, v129
	v_fmac_f32_e32 v89, v30, v126
	v_med3_f32 v91, v91, s35, v109
	v_med3_f32 v45, v89, s35, v109
	v_med3_f32 v88, v88, s35, v109
	v_cvt_pk_fp8_f32 v86, v91, v94 op_sel:[0,0,1]
	v_cvt_pk_fp8_f32 v87, v45, v88 op_sel:[0,0,1]
	v_lshlrev_b32_e32 v121, 16, v38
	v_and_b32_e32 v122, 0xffff0000, v38
	v_lshlrev_b32_e32 v90, 16, v39
	global_store_dwordx2 v[42:43], v[86:87], off offset:-1280
	v_and_b32_e32 v91, 0xffff0000, v39
	v_lshlrev_b32_e32 v88, 16, v40
	v_and_b32_e32 v89, 0xffff0000, v40
	v_lshlrev_b32_e32 v86, 16, v41
	v_and_b32_e32 v87, 0xffff0000, v41

.LBB0_1041:
	s_or_b64 exec, exec, s[18:19]
	v_mov_b32_e32 v18, v204
	v_mov_b32_e32 v19, v205
	v_mov_b32_e32 v20, v206
	v_mov_b32_e32 v21, v207
	v_mov_b32_e32 v22, 0
	v_mov_b32_e32 v23, 0
	v_lshlrev_b32_e32 v24, 16, v18
	v_and_b32_e32 v18, 0xffff0000, v18
	v_lshlrev_b32_e32 v26, 16, v20
	v_and_b32_e32 v20, 0xffff0000, v20
	v_mul_f32_e32 v24, v46, v24
	v_mul_f32_e32 v18, v46, v18
	v_mul_f32_e32 v26, v46, v26
	v_mul_f32_e32 v20, v46, v20
	v_med3_f32 v24, v24, s35, v109
	v_med3_f32 v18, v18, s35, v109
	v_med3_f32 v26, v26, s35, v109
	v_med3_f32 v20, v20, s35, v109
	v_cvt_pk_fp8_f32 v22, v24, v18
	v_cvt_pk_fp8_f32 v23, v26, v20
	v_lshlrev_b32_e32 v25, 16, v19
	v_and_b32_e32 v19, 0xffff0000, v19
	v_lshlrev_b32_e32 v27, 16, v21
	v_and_b32_e32 v21, 0xffff0000, v21
	v_mul_f32_e32 v25, v46, v25
	v_mul_f32_e32 v19, v46, v19
	v_mul_f32_e32 v27, v46, v27
	v_mul_f32_e32 v21, v46, v21
	v_med3_f32 v25, v25, s35, v109
	v_med3_f32 v19, v19, s35, v109
	v_med3_f32 v18, v27, s35, v109
	v_med3_f32 v20, v21, s35, v109
	v_cvt_pk_fp8_f32 v22, v25, v19 op_sel:[0,0,1]
	v_cvt_pk_fp8_f32 v23, v18, v20 op_sel:[0,0,1]
	ds_write_b64 v116, v[22:23]
	s_and_saveexec_b64 s[18:19], s[16:17]
	s_cbranch_execz .LBB0_998
	v_mov_b32_e32 v18, v208
	v_mov_b32_e32 v19, v209
	v_mov_b32_e32 v20, v210
	v_mov_b32_e32 v21, v211
	v_mov_b32_e32 v22, v47
	v_mov_b32_e32 v23, v47
	v_lshlrev_b32_e32 v24, 16, v18
	v_and_b32_e32 v18, 0xffff0000, v18
	v_lshlrev_b32_e32 v26, 16, v20
	v_and_b32_e32 v20, 0xffff0000, v20
	v_mul_f32_e32 v24, v46, v24
	v_mul_f32_e32 v18, v46, v18
	v_mul_f32_e32 v26, v46, v26
	v_mul_f32_e32 v20, v46, v20
	v_med3_f32 v24, v24, s35, v109
	v_med3_f32 v18, v18, s35, v109
	v_med3_f32 v26, v26, s35, v109
	v_med3_f32 v20, v20, s35, v109
	v_cvt_pk_fp8_f32 v22, v24, v18
	v_cvt_pk_fp8_f32 v23, v26, v20
	v_lshlrev_b32_e32 v25, 16, v19
	v_and_b32_e32 v19, 0xffff0000, v19
	v_lshlrev_b32_e32 v27, 16, v21
	v_and_b32_e32 v21, 0xffff0000, v21
	v_mul_f32_e32 v25, v46, v25
	v_mul_f32_e32 v19, v46, v19
	v_mul_f32_e32 v27, v46, v27
	v_mul_f32_e32 v21, v46, v21
	v_med3_f32 v25, v25, s35, v109
	v_med3_f32 v19, v19, s35, v109
	v_med3_f32 v18, v27, s35, v109
	v_med3_f32 v20, v21, s35, v109
	v_cvt_pk_fp8_f32 v22, v25, v19 op_sel:[0,0,1]
	v_cvt_pk_fp8_f32 v23, v18, v20 op_sel:[0,0,1]
	ds_write_b64 v116, v[22:23] offset:512
	s_branch .LBB0_998

.LBB0_2106:
	s_or_b64 exec, exec, s[20:21]
	v_mov_b32_e32 v192, 0
	v_mov_b32_e32 v193, 0
	v_mov_b32_e32 v194, 0
	v_mov_b32_e32 v195, 0
	v_mov_b32_e32 v196, 0
	v_mov_b32_e32 v197, 0
	v_mov_b32_e32 v198, 0
	v_mov_b32_e32 v199, 0
	v_mov_b32_e32 v200, 0
	v_mov_b32_e32 v201, 0
	v_mov_b32_e32 v202, 0
	v_mov_b32_e32 v203, 0
	v_lshl_add_u64 v[212:213], s[86:87], 0, v[78:79]
	v_lshl_add_u64 v[214:215], s[86:87], 0, v[72:73]
	s_and_saveexec_b64 s[42:43], s[6:7]
	s_and_saveexec_b64 s[44:45], s[10:11]
	s_xor_b64 s[44:45], exec, s[44:45]
	global_load_dwordx4 v[192:195], v[212:213], off offset:-1280
	global_load_dwordx4 v[196:199], v[212:213], off
	global_load_dwordx4 v[200:203], v[212:213], off offset:1280
	s_andn2_saveexec_b64 s[44:45], s[44:45]
	global_load_dwordx4 v[192:195], v[214:215], off
	global_load_dwordx4 v[196:199], v[214:215], off
	global_load_dwordx4 v[200:203], v[214:215], off
	s_or_b64 exec, exec, s[44:45]
	s_or_b64 exec, exec, s[42:43]
	v_lshl_add_u64 v[216:217], s[86:87], 0, v[82:83]
	global_load_dwordx4 v[204:207], v[216:217], off
	v_lshl_add_u64 v[216:217], s[86:87], 0, v[80:81]
	s_and_saveexec_b64 s[42:43], s[16:17]
	global_load_dwordx4 v[208:211], v[216:217], off
	s_or_b64 exec, exec, s[42:43]
	s_waitcnt lgkmcnt(0)
	v_pk_add_f32 v[34:35], v[34:35], v[36:37]
	s_andn2_b64 vcc, exec, s[18:19]
	v_pk_fma_f32 v[86:87], v[34:35], s[2:3], v[68:69] op_sel_hi:[1,0,0]
	s_nop 0
	v_cmp_gt_f32_e64 s[20:21], s37, v87
	v_cmp_gt_f32_e64 s[18:19], s37, v86
	s_cbranch_vccnz .Lmy_skipq_l1
	v_mov_b32_e32 v38, 0
	v_lshl_add_u64 v[88:89], s[86:87], 0, v[70:71]
	v_mov_b32_e32 v42, 0
	v_mov_b32_e32 v43, 0
	v_mov_b32_e32 v44, 0
	v_mov_b32_e32 v45, 0
	s_and_saveexec_b64 s[28:29], s[6:7]
	s_cbranch_execz .LBB0_2109
	global_load_dwordx4 v[42:45], v[88:89], off offset:-768

.LBB0_2122:
	s_waitcnt lgkmcnt(1)
	v_mov_b32_e32 v42, v192
	v_mov_b32_e32 v43, v193
	v_mov_b32_e32 v44, v194
	v_mov_b32_e32 v45, v195
	v_mov_b32_e32 v38, v196
	v_mov_b32_e32 v39, v197
	v_mov_b32_e32 v40, v198
	v_mov_b32_e32 v41, v199
	v_mov_b32_e32 v34, v200
	v_mov_b32_e32 v35, v201
	v_mov_b32_e32 v36, v202
	v_mov_b32_e32 v37, v203
	v_mov_b32_e32 v87, 0
	v_mov_b32_e32 v114, 0
	v_mov_b32_e32 v92, 0
	v_mov_b32_e32 v93, 0
	v_mov_b32_e32 v90, 0
	s_waitcnt lgkmcnt(0)
	v_mov_b32_e32 v91, 0
	v_mov_b32_e32 v88, 0
	v_mov_b32_e32 v89, 0
	s_and_saveexec_b64 s[20:21], s[6:7]
	s_cbranch_execz .LBB0_2142
	v_lshlrev_b32_e32 v87, 16, v42
	v_and_b32_e32 v114, 0xffff0000, v42
	v_lshlrev_b32_e32 v92, 16, v43
	v_and_b32_e32 v93, 0xffff0000, v43
	v_lshlrev_b32_e32 v90, 16, v44
	v_and_b32_e32 v91, 0xffff0000, v44
	v_lshlrev_b32_e32 v88, 16, v45
	v_and_b32_e32 v89, 0xffff0000, v45
.LBB0_2142:
	s_or_b64 exec, exec, s[20:21]
	v_mul_f32_e32 v42, 0x4b800000, v86
	v_cndmask_b32_e64 v42, v86, v42, s[18:19]
	v_rsq_f32_e32 v42, v42
	s_nop 0
	v_mul_f32_e32 v43, 0x45800000, v42
	v_cndmask_b32_e64 v46, v42, v43, s[18:19]
	v_cndmask_b32_e64 v44, v46, 1.0, s[8:9]
	v_mul_f32_e32 v45, v44, v87
	v_mul_f32_e32 v114, v44, v114
	v_pk_mul_f32 v[42:43], v[44:45], v[92:93] op_sel_hi:[0,1]
	v_mul_f32_e32 v92, v114, v114
	v_pk_mul_f32 v[86:87], v[42:43], v[42:43]
	v_fmac_f32_e32 v92, v45, v45
	v_add_f32_e32 v86, v86, v92
	v_add_f32_e32 v92, v87, v86
	v_pk_mul_f32 v[86:87], v[44:45], v[90:91] op_sel_hi:[0,1]
	v_pk_mul_f32 v[90:91], v[86:87], v[86:87]
	v_pk_mul_f32 v[88:89], v[44:45], v[88:89] op_sel_hi:[0,1]
	v_add_f32_e32 v90, v90, v92
	v_add_f32_e32 v92, v91, v90
	v_pk_mul_f32 v[90:91], v[88:89], v[88:89]
	s_nop 0
	v_add_f32_e32 v90, v90, v92
	v_add_f32_e32 v90, v91, v90
	ds_bpermute_b32 v91, v107, v90
	s_waitcnt lgkmcnt(0)
	v_add_f32_e32 v90, v90, v91
	ds_bpermute_b32 v91, v108, v90
	s_waitcnt lgkmcnt(0)
	v_add_f32_e32 v90, v90, v91
	ds_bpermute_b32 v91, v109, v90
	s_waitcnt lgkmcnt(0)
	v_add_f32_e32 v90, v90, v91
	ds_bpermute_b32 v91, v110, v90
	s_waitcnt lgkmcnt(0)
	v_add_f32_e32 v90, v90, v91
	ds_bpermute_b32 v91, v111, v90
	s_waitcnt lgkmcnt(0)
	v_add_f32_e32 v90, v90, v91
	v_fmamk_f32 v90, v90, 0x3baaaaab, v68
	v_mul_f32_e32 v91, 0x4b800000, v90
	v_cmp_gt_f32_e32 vcc, s37, v90
	s_nop 1
	v_cndmask_b32_e32 v90, v90, v91, vcc
	v_rsq_f32_e32 v90, v90
	s_nop 0
	v_mul_f32_e32 v91, 0x45800000, v90
	v_cndmask_b32_e32 v90, v90, v91, vcc
	v_mul_f32_e32 v90, 0x3ea535b8, v90
	v_mul_f32_e32 v115, v16, v90
	v_mul_f32_e32 v91, v14, v90
	v_mul_f32_e32 v92, v15, v90
	v_mul_f32_e32 v116, v17, v90
	v_mul_f32_e32 v118, v6, v90
	v_mul_f32_e32 v120, v7, v90
	v_mul_f32_e32 v121, v8, v90
	v_mul_f32_e32 v115, v42, v115
	v_mul_f32_e32 v42, v9, v90
	v_mul_f32_e32 v45, v45, v91
	v_mul_f32_e32 v93, v114, v92
	v_mul_f32_e32 v117, v43, v116
	v_mul_f32_e32 v119, v86, v118
	v_mul_f32_e32 v123, v87, v120
	v_mul_f32_e32 v125, v88, v121
	v_mul_f32_e32 v128, v89, v42
	ds_bpermute_b32 v114, v108, v45
	ds_bpermute_b32 v116, v108, v93
	ds_bpermute_b32 v118, v108, v115
	ds_bpermute_b32 v122, v108, v117
	ds_bpermute_b32 v124, v108, v119
	ds_bpermute_b32 v126, v108, v123
	ds_bpermute_b32 v127, v108, v125
	ds_bpermute_b32 v129, v108, v128
	v_mov_b32_e32 v92, 0
	v_lshl_add_u64 v[42:43], s[86:87], 0, v[84:85]
	v_mov_b32_e32 v120, 0
	v_mov_b32_e32 v121, 0
	v_mov_b32_e32 v90, 0
	v_mov_b32_e32 v91, 0
	v_mov_b32_e32 v88, 0
	v_mov_b32_e32 v89, 0
	v_mov_b32_e32 v86, 0
	v_mov_b32_e32 v87, 0
	s_and_saveexec_b64 s[18:19], s[6:7]
	s_cbranch_execz .LBB0_2144
	s_waitcnt lgkmcnt(0)
	v_mul_f32_e32 v86, v33, v129
	v_mul_f32_e32 v91, v23, v118
	v_cndmask_b32_e64 v88, v86, -v86, s[12:13]
	v_mul_f32_e32 v86, v31, v127
	v_cndmask_b32_e64 v91, v91, -v91, s[12:13]
	v_cndmask_b32_e64 v89, v86, -v86, s[12:13]
	v_mul_f32_e32 v86, v29, v126
	v_fmac_f32_e32 v91, v22, v115
	v_mul_f32_e32 v115, v21, v116
	v_cndmask_b32_e64 v87, v86, -v86, s[12:13]
	v_mul_f32_e32 v86, v27, v124
	v_cndmask_b32_e64 v115, v115, -v115, s[12:13]
	v_cndmask_b32_e64 v90, v86, -v86, s[12:13]
	v_mul_f32_e32 v86, v25, v122
	v_fmac_f32_e32 v115, v20, v93
	v_mul_f32_e32 v93, v19, v114
	v_cndmask_b32_e64 v86, v86, -v86, s[12:13]
	v_cndmask_b32_e64 v93, v93, -v93, s[12:13]
	v_fmac_f32_e32 v86, v24, v117
	v_fmac_f32_e32 v93, v18, v45
	v_fmac_f32_e32 v87, v28, v123
	v_fmac_f32_e32 v90, v26, v119
	v_med3_f32 v45, v93, s38, v106
	v_med3_f32 v93, v115, s38, v106
	v_med3_f32 v114, v86, s38, v106
	v_mov_b32_e32 v86, v47
	v_cvt_pk_fp8_f32 v86, v45, v93
	v_med3_f32 v45, v90, s38, v106
	v_med3_f32 v90, v87, s38, v106
	v_mov_b32_e32 v87, v47
	v_cvt_pk_fp8_f32 v87, v45, v90
	v_fmac_f32_e32 v88, v32, v128
	v_fmac_f32_e32 v89, v30, v125
	v_med3_f32 v91, v91, s38, v106
	v_med3_f32 v45, v89, s38, v106
	v_med3_f32 v88, v88, s38, v106
	v_cvt_pk_fp8_f32 v86, v91, v114 op_sel:[0,0,1]
	v_cvt_pk_fp8_f32 v87, v45, v88 op_sel:[0,0,1]
	v_lshlrev_b32_e32 v120, 16, v38
	v_and_b32_e32 v121, 0xffff0000, v38
	v_lshlrev_b32_e32 v90, 16, v39
	global_store_dwordx2 v[42:43], v[86:87], off offset:-1280
	v_and_b32_e32 v91, 0xffff0000, v39
	v_lshlrev_b32_e32 v88, 16, v40
	v_and_b32_e32 v89, 0xffff0000, v40
	v_lshlrev_b32_e32 v86, 16, v41
	v_and_b32_e32 v87, 0xffff0000, v41

.LBB0_2148:
	s_or_b64 exec, exec, s[18:19]
	v_mov_b32_e32 v18, v204
	v_mov_b32_e32 v19, v205
	v_mov_b32_e32 v20, v206
	v_mov_b32_e32 v21, v207
	v_mov_b32_e32 v22, 0
	v_mov_b32_e32 v23, 0
	v_lshlrev_b32_e32 v24, 16, v18
	v_and_b32_e32 v18, 0xffff0000, v18
	v_lshlrev_b32_e32 v26, 16, v20
	v_and_b32_e32 v20, 0xffff0000, v20
	v_mul_f32_e32 v24, v46, v24
	v_mul_f32_e32 v18, v46, v18
	v_mul_f32_e32 v26, v46, v26
	v_mul_f32_e32 v20, v46, v20
	v_med3_f32 v24, v24, s38, v106
	v_med3_f32 v18, v18, s38, v106
	v_med3_f32 v26, v26, s38, v106
	v_med3_f32 v20, v20, s38, v106
	v_cvt_pk_fp8_f32 v22, v24, v18
	v_cvt_pk_fp8_f32 v23, v26, v20
	v_lshlrev_b32_e32 v25, 16, v19
	v_and_b32_e32 v19, 0xffff0000, v19
	v_lshlrev_b32_e32 v27, 16, v21
	v_and_b32_e32 v21, 0xffff0000, v21
	v_mul_f32_e32 v25, v46, v25
	v_mul_f32_e32 v19, v46, v19
	v_mul_f32_e32 v27, v46, v27
	v_mul_f32_e32 v21, v46, v21
	v_med3_f32 v25, v25, s38, v106
	v_med3_f32 v19, v19, s38, v106
	v_med3_f32 v18, v27, s38, v106
	v_med3_f32 v20, v21, s38, v106
	v_cvt_pk_fp8_f32 v22, v25, v19 op_sel:[0,0,1]
	v_cvt_pk_fp8_f32 v23, v18, v20 op_sel:[0,0,1]
	ds_write_b64 v113, v[22:23]
	s_and_saveexec_b64 s[18:19], s[16:17]
	s_cbranch_execz .LBB0_2103
	v_mov_b32_e32 v18, v208
	v_mov_b32_e32 v19, v209
	v_mov_b32_e32 v20, v210
	v_mov_b32_e32 v21, v211
	v_mov_b32_e32 v22, v47
	v_mov_b32_e32 v23, v47
	v_lshlrev_b32_e32 v24, 16, v18
	v_and_b32_e32 v18, 0xffff0000, v18
	v_lshlrev_b32_e32 v26, 16, v20
	v_and_b32_e32 v20, 0xffff0000, v20
	v_mul_f32_e32 v24, v46, v24
	v_mul_f32_e32 v18, v46, v18
	v_mul_f32_e32 v26, v46, v26
	v_mul_f32_e32 v20, v46, v20
	v_med3_f32 v24, v24, s38, v106
	v_med3_f32 v18, v18, s38, v106
	v_med3_f32 v26, v26, s38, v106
	v_med3_f32 v20, v20, s38, v106
	v_cvt_pk_fp8_f32 v22, v24, v18
	v_cvt_pk_fp8_f32 v23, v26, v20
	v_lshlrev_b32_e32 v25, 16, v19
	v_and_b32_e32 v19, 0xffff0000, v19
	v_lshlrev_b32_e32 v27, 16, v21
	v_and_b32_e32 v21, 0xffff0000, v21
	v_mul_f32_e32 v25, v46, v25
	v_mul_f32_e32 v19, v46, v19
	v_mul_f32_e32 v27, v46, v27
	v_mul_f32_e32 v21, v46, v21
	v_med3_f32 v25, v25, s38, v106
	v_med3_f32 v19, v19, s38, v106
	v_med3_f32 v18, v27, s38, v106
	v_med3_f32 v20, v21, s38, v106
	v_cvt_pk_fp8_f32 v22, v25, v19 op_sel:[0,0,1]
	v_cvt_pk_fp8_f32 v23, v18, v20 op_sel:[0,0,1]
	ds_write_b64 v113, v[22:23] offset:512
	s_branch .LBB0_2103
.Lmy_skipq_l1:
	s_waitcnt vmcnt(0)
	s_branch .LBB0_2122
